# phi-copy elimination: sparse attention query loop unrolled 2x with the current/next K,V register sets swapped in the second copy (32 v_mov_b64 per step removed)
# baseline (speedup 1.0000x reference)
.LBB0_1387:
	ds_read_b128 v[160:163], v246
	v_mfma_f32_16x16x32_fp8_fp8 v[164:167], v[8:9], v[174:175], 0
	s_andn2_b64 vcc, exec, s[28:29]
	s_waitcnt lgkmcnt(0)
	v_add_u32_e32 v2, v211, v160
	v_add_u32_e32 v160, v211, v161
	v_add_u32_e32 v161, v211, v162
	v_add_u32_e32 v162, v211, v163
	ds_read_b32 v168, v2 offset:8192
	ds_read_b32 v169, v160 offset:8192
	ds_read_b32 v170, v161 offset:8192
	ds_read_b32 v171, v162 offset:8192
	v_mfma_f32_16x16x32_fp8_fp8 v[160:163], v[10:11], v[176:177], v[164:167]
	s_waitcnt lgkmcnt(2)
	s_nop 6
	v_pk_fma_f32 v[160:161], v[160:161], s[72:73], v[168:169] op_sel_hi:[1,0,1]
	s_waitcnt lgkmcnt(0)
	v_pk_fma_f32 v[162:163], v[162:163], s[72:73], v[170:171] op_sel_hi:[1,0,1]
	s_nop 0
	ds_read_b128 v[164:167], v246 offset:64
	s_waitcnt lgkmcnt(0)
	v_add_u32_e32 v2, v211, v164
	v_add_u32_e32 v169, v211, v165
	v_add_u32_e32 v170, v211, v166
	v_add_u32_e32 v171, v211, v167
	v_mfma_f32_16x16x32_fp8_fp8 v[164:167], v[4:5], v[174:175], 0
	ds_read_b32 v168, v2 offset:8192
	ds_read_b32 v169, v169 offset:8192
	ds_read_b32 v170, v170 offset:8192
	ds_read_b32 v171, v171 offset:8192
	v_mfma_f32_16x16x32_fp8_fp8 v[164:167], v[6:7], v[176:177], v[164:167]
	s_waitcnt lgkmcnt(0)
	s_nop 6
	v_pk_fma_f32 v[166:167], v[166:167], s[72:73], v[170:171] op_sel_hi:[1,0,1]
	v_pk_fma_f32 v[164:165], v[164:165], s[72:73], v[168:169] op_sel_hi:[1,0,1]
	s_nop 0
	ds_read_b128 v[178:181], v246 offset:128
	s_waitcnt lgkmcnt(0)
	v_add_u32_e32 v2, v211, v178
	v_add_u32_e32 v169, v211, v179
	v_add_u32_e32 v170, v211, v180
	v_add_u32_e32 v171, v211, v181
	v_mfma_f32_16x16x32_fp8_fp8 v[178:181], v[16:17], v[174:175], 0
	ds_read_b32 v168, v2 offset:8192
	ds_read_b32 v169, v169 offset:8192
	ds_read_b32 v170, v170 offset:8192
	ds_read_b32 v171, v171 offset:8192
	v_mfma_f32_16x16x32_fp8_fp8 v[178:181], v[18:19], v[176:177], v[178:181]
	s_waitcnt lgkmcnt(0)
	s_nop 6
	v_pk_fma_f32 v[180:181], v[180:181], s[72:73], v[170:171] op_sel_hi:[1,0,1]
	v_pk_fma_f32 v[178:179], v[178:179], s[72:73], v[168:169] op_sel_hi:[1,0,1]
	s_nop 0
	ds_read_b128 v[182:185], v246 offset:192
	s_waitcnt lgkmcnt(0)
	v_add_u32_e32 v2, v211, v182
	v_add_u32_e32 v169, v211, v183
	v_add_u32_e32 v170, v211, v184
	v_add_u32_e32 v171, v211, v185
	v_mfma_f32_16x16x32_fp8_fp8 v[182:185], v[12:13], v[174:175], 0
	ds_read_b32 v168, v2 offset:8192
	ds_read_b32 v169, v169 offset:8192
	ds_read_b32 v170, v170 offset:8192
	ds_read_b32 v171, v171 offset:8192
	v_max3_f32 v2, v160, s33, v161
	v_max3_f32 v2, v2, v162, v163
	v_mfma_f32_16x16x32_fp8_fp8 v[182:185], v[14:15], v[176:177], v[182:185]
	v_max3_f32 v2, v2, v164, v165
	v_max3_f32 v2, v2, v166, v167
	v_max3_f32 v2, v2, v178, v179
	v_max3_f32 v2, v2, v180, v181
	s_waitcnt lgkmcnt(0)
	s_nop 2
	v_pk_fma_f32 v[184:185], v[184:185], s[72:73], v[170:171] op_sel_hi:[1,0,1]
	v_pk_fma_f32 v[182:183], v[182:183], s[72:73], v[168:169] op_sel_hi:[1,0,1]
	s_nop 0
	ds_read_b128 v[186:189], v246 offset:256
	v_max3_f32 v2, v2, v182, v183
	v_max3_f32 v2, v2, v184, v185
	s_waitcnt lgkmcnt(0)
	v_add_u32_e32 v168, v211, v186
	v_add_u32_e32 v169, v211, v187
	v_add_u32_e32 v170, v211, v188
	v_add_u32_e32 v171, v211, v189
	v_mfma_f32_16x16x32_fp8_fp8 v[186:189], v[24:25], v[174:175], 0
	ds_read_b32 v168, v168 offset:8192
	ds_read_b32 v169, v169 offset:8192
	ds_read_b32 v170, v170 offset:8192
	ds_read_b32 v171, v171 offset:8192
	v_mfma_f32_16x16x32_fp8_fp8 v[186:189], v[26:27], v[176:177], v[186:189]
	s_waitcnt lgkmcnt(0)
	s_nop 6
	v_pk_fma_f32 v[236:237], v[188:189], s[72:73], v[170:171] op_sel_hi:[1,0,1]
	v_pk_fma_f32 v[234:235], v[186:187], s[72:73], v[168:169] op_sel_hi:[1,0,1]
	s_nop 0
	ds_read_b128 v[186:189], v246 offset:320
	v_max3_f32 v2, v2, v234, v235
	v_max3_f32 v2, v2, v236, v237
	s_waitcnt lgkmcnt(0)
	v_add_u32_e32 v168, v211, v186
	v_add_u32_e32 v169, v211, v187
	v_add_u32_e32 v170, v211, v188
	v_add_u32_e32 v171, v211, v189
	v_mfma_f32_16x16x32_fp8_fp8 v[186:189], v[20:21], v[174:175], 0
	ds_read_b32 v168, v168 offset:8192
	ds_read_b32 v169, v169 offset:8192
	ds_read_b32 v170, v170 offset:8192
	ds_read_b32 v171, v171 offset:8192
	v_mfma_f32_16x16x32_fp8_fp8 v[186:189], v[22:23], v[176:177], v[186:189]
	s_waitcnt lgkmcnt(0)
	s_nop 6
	v_pk_fma_f32 v[230:231], v[188:189], s[72:73], v[170:171] op_sel_hi:[1,0,1]
	v_pk_fma_f32 v[228:229], v[186:187], s[72:73], v[168:169] op_sel_hi:[1,0,1]
	s_nop 0
	ds_read_b128 v[186:189], v246 offset:384
	v_max3_f32 v2, v2, v228, v229
	v_max3_f32 v2, v2, v230, v231
	s_waitcnt lgkmcnt(0)
	v_add_u32_e32 v168, v211, v186
	v_add_u32_e32 v169, v211, v187
	v_add_u32_e32 v170, v211, v188
	v_add_u32_e32 v171, v211, v189
	v_mfma_f32_16x16x32_fp8_fp8 v[186:189], v[32:33], v[174:175], 0
	ds_read_b32 v168, v168 offset:8192
	ds_read_b32 v169, v169 offset:8192
	ds_read_b32 v170, v170 offset:8192
	ds_read_b32 v171, v171 offset:8192
	v_mfma_f32_16x16x32_fp8_fp8 v[186:189], v[34:35], v[176:177], v[186:189]
	s_waitcnt lgkmcnt(0)
	s_nop 6
	v_pk_fma_f32 v[170:171], v[188:189], s[72:73], v[170:171] op_sel_hi:[1,0,1]
	v_pk_fma_f32 v[168:169], v[186:187], s[72:73], v[168:169] op_sel_hi:[1,0,1]
	s_nop 0
	ds_read_b128 v[186:189], v246 offset:448
	v_max3_f32 v2, v2, v168, v169
	v_max3_f32 v2, v2, v170, v171
	s_waitcnt lgkmcnt(0)
	v_add_u32_e32 v190, v211, v186
	v_add_u32_e32 v191, v211, v187
	v_add_u32_e32 v192, v211, v188
	v_add_u32_e32 v193, v211, v189
	v_mfma_f32_16x16x32_fp8_fp8 v[186:189], v[28:29], v[174:175], 0
	ds_read_b32 v190, v190 offset:8192
	ds_read_b32 v191, v191 offset:8192
	ds_read_b32 v192, v192 offset:8192
	ds_read_b32 v193, v193 offset:8192
	v_mfma_f32_16x16x32_fp8_fp8 v[186:189], v[30:31], v[176:177], v[186:189]
	s_waitcnt lgkmcnt(0)
	s_nop 6
	v_pk_fma_f32 v[218:219], v[188:189], s[72:73], v[192:193] op_sel_hi:[1,0,1]
	v_pk_fma_f32 v[216:217], v[186:187], s[72:73], v[190:191] op_sel_hi:[1,0,1]
	s_nop 0
	s_nop 0
	v_max3_f32 v2, v2, v216, v217
	v_max3_f32 v2, v2, v218, v219
	v_mov_b32_e32 v186, v2
	s_nop 1
	v_permlane16_swap_b32_e32 v2, v186
	v_max_f32_e32 v186, v186, v186
	v_max_f32_e32 v2, v2, v2
	v_max_f32_e32 v2, v2, v186
	v_mov_b32_e32 v186, v2
	s_nop 1
	v_permlane32_swap_b32_e32 v2, v186
	v_max3_f32 v214, v196, v2, v186
	v_sub_f32_e32 v163, v163, v214
	v_sub_f32_e32 v162, v162, v214
	v_sub_f32_e32 v161, v161, v214
	v_sub_f32_e32 v160, v160, v214
	v_sub_f32_e32 v2, v196, v214
	v_exp_f32_e32 v196, v160
	v_exp_f32_e32 v197, v161
	v_exp_f32_e32 v198, v162
	v_exp_f32_e32 v199, v163
	v_sub_f32_e32 v163, v167, v214
	v_sub_f32_e32 v162, v166, v214
	v_sub_f32_e32 v161, v165, v214
	v_sub_f32_e32 v160, v164, v214
	v_sub_f32_e32 v167, v219, v214
	v_exp_f32_e32 v200, v160
	v_exp_f32_e32 v201, v161
	v_exp_f32_e32 v202, v162
	v_exp_f32_e32 v203, v163
	v_sub_f32_e32 v163, v181, v214
	v_sub_f32_e32 v162, v180, v214
	v_sub_f32_e32 v161, v179, v214
	v_sub_f32_e32 v160, v178, v214
	v_sub_f32_e32 v166, v218, v214
	v_exp_f32_e32 v188, v160
	v_exp_f32_e32 v189, v161
	v_exp_f32_e32 v190, v162
	v_exp_f32_e32 v191, v163
	v_sub_f32_e32 v163, v185, v214
	v_sub_f32_e32 v162, v184, v214
	v_sub_f32_e32 v161, v183, v214
	v_sub_f32_e32 v160, v182, v214
	v_sub_f32_e32 v165, v217, v214
	v_exp_f32_e32 v192, v160
	v_exp_f32_e32 v193, v161
	v_exp_f32_e32 v194, v162
	v_exp_f32_e32 v195, v163
	v_sub_f32_e32 v163, v237, v214
	v_sub_f32_e32 v162, v236, v214
	v_sub_f32_e32 v161, v235, v214
	v_sub_f32_e32 v160, v234, v214
	v_sub_f32_e32 v164, v216, v214
	v_exp_f32_e32 v178, v160
	v_exp_f32_e32 v179, v161
	v_exp_f32_e32 v180, v162
	v_exp_f32_e32 v181, v163
	v_sub_f32_e32 v163, v231, v214
	v_sub_f32_e32 v162, v230, v214
	v_sub_f32_e32 v161, v229, v214
	v_sub_f32_e32 v160, v228, v214
	v_pk_add_f32 v[218:219], v[190:191], v[194:195]
	v_exp_f32_e32 v182, v160
	v_exp_f32_e32 v183, v161
	v_exp_f32_e32 v184, v162
	v_exp_f32_e32 v185, v163
	v_sub_f32_e32 v163, v171, v214
	v_sub_f32_e32 v162, v170, v214
	v_sub_f32_e32 v161, v169, v214
	v_sub_f32_e32 v160, v168, v214
	v_pk_add_f32 v[170:171], v[198:199], v[202:203]
	v_exp_f32_e32 v160, v160
	v_exp_f32_e32 v161, v161
	v_exp_f32_e32 v162, v162
	v_exp_f32_e32 v163, v163
	v_exp_f32_e32 v164, v164
	v_exp_f32_e32 v165, v165
	v_exp_f32_e32 v166, v166
	v_exp_f32_e32 v167, v167
	v_pk_add_f32 v[168:169], v[196:197], v[200:201]
	v_pk_add_f32 v[216:217], v[188:189], v[192:193]
	v_pk_add_f32 v[230:231], v[180:181], v[184:185]
	v_pk_add_f32 v[228:229], v[178:179], v[182:183]
	v_pk_add_f32 v[236:237], v[162:163], v[166:167]
	v_pk_add_f32 v[234:235], v[160:161], v[164:165]
	v_exp_f32_e32 v2, v2
	s_nop 0
	v_pk_add_f32 v[170:171], v[170:171], v[218:219]
	v_pk_add_f32 v[168:169], v[168:169], v[216:217]
	v_pk_add_f32 v[218:219], v[230:231], v[236:237]
	v_pk_add_f32 v[216:217], v[228:229], v[234:235]
	v_pk_mul_f32 v[158:159], v[158:159], v[2:3] op_sel_hi:[1,0]
	v_pk_mul_f32 v[156:157], v[156:157], v[2:3] op_sel_hi:[1,0]
	v_pk_add_f32 v[170:171], v[170:171], v[218:219]
	v_pk_add_f32 v[168:169], v[168:169], v[216:217]
	v_cvt_scalef32_pk_bf16_fp8 v217, v42, 1.0 op_sel:[1,0,0]
	v_cvt_scalef32_pk_bf16_fp8 v216, v42, 1.0
	v_pk_add_f32 v[186:187], v[168:169], v[170:171]
	v_cvt_scalef32_pk_bf16_fp8 v169, v40, 1.0 op_sel:[1,0,0]
	v_cvt_scalef32_pk_bf16_fp8 v168, v40, 1.0
	v_cvt_scalef32_pk_bf16_fp8 v171, v41, 1.0 op_sel:[1,0,0]
	v_cvt_scalef32_pk_bf16_fp8 v170, v41, 1.0
	v_cvt_scalef32_pk_bf16_fp8 v218, v43, 1.0
	v_cvt_scalef32_pk_bf16_fp8 v219, v43, 1.0 op_sel:[1,0,0]
	ds_write_b128 v220, v[168:171] offset:43264
	ds_write_b128 v220, v[216:219] offset:43280
	v_cvt_scalef32_pk_bf16_fp8 v169, v36, 1.0 op_sel:[1,0,0]
	v_cvt_scalef32_pk_bf16_fp8 v168, v36, 1.0
	v_cvt_scalef32_pk_bf16_fp8 v171, v37, 1.0 op_sel:[1,0,0]
	v_cvt_scalef32_pk_bf16_fp8 v170, v37, 1.0
	v_cvt_scalef32_pk_bf16_fp8 v217, v38, 1.0 op_sel:[1,0,0]
	v_cvt_scalef32_pk_bf16_fp8 v216, v38, 1.0
	v_cvt_scalef32_pk_bf16_fp8 v218, v39, 1.0
	v_cvt_scalef32_pk_bf16_fp8 v219, v39, 1.0 op_sel:[1,0,0]
	ds_write_b128 v220, v[168:171] offset:43776
	ds_write_b128 v220, v[216:219] offset:43792
	v_cvt_scalef32_pk_bf16_fp8 v169, v48, 1.0 op_sel:[1,0,0]
	v_cvt_scalef32_pk_bf16_fp8 v168, v48, 1.0
	v_cvt_scalef32_pk_bf16_fp8 v171, v49, 1.0 op_sel:[1,0,0]
	v_cvt_scalef32_pk_bf16_fp8 v170, v49, 1.0
	v_cvt_scalef32_pk_bf16_fp8 v217, v50, 1.0 op_sel:[1,0,0]
	v_cvt_scalef32_pk_bf16_fp8 v216, v50, 1.0
	v_cvt_scalef32_pk_bf16_fp8 v218, v51, 1.0
	v_cvt_scalef32_pk_bf16_fp8 v219, v51, 1.0 op_sel:[1,0,0]
	ds_write_b128 v220, v[168:171] offset:44288
	ds_write_b128 v220, v[216:219] offset:44304
	v_cvt_scalef32_pk_bf16_fp8 v169, v44, 1.0 op_sel:[1,0,0]
	v_cvt_scalef32_pk_bf16_fp8 v168, v44, 1.0
	v_cvt_scalef32_pk_bf16_fp8 v171, v45, 1.0 op_sel:[1,0,0]
	v_cvt_scalef32_pk_bf16_fp8 v170, v45, 1.0
	v_cvt_scalef32_pk_bf16_fp8 v217, v46, 1.0 op_sel:[1,0,0]
	v_cvt_scalef32_pk_bf16_fp8 v216, v46, 1.0
	v_cvt_scalef32_pk_bf16_fp8 v218, v47, 1.0
	v_cvt_scalef32_pk_bf16_fp8 v219, v47, 1.0 op_sel:[1,0,0]
	ds_write_b128 v220, v[168:171] offset:44800
	ds_write_b128 v220, v[216:219] offset:44816
	v_cvt_pk_bf16_f32 v168, v196, v197
	v_cvt_pk_bf16_f32 v169, v198, v199
	v_cvt_pk_bf16_f32 v170, v200, v201
	v_cvt_pk_bf16_f32 v171, v202, v203
	ds_read_b64_tr_b16 v[196:197], v221 offset:43264
	ds_read_b64_tr_b16 v[198:199], v221 offset:43776
	ds_read_b64_tr_b16 v[200:201], v221 offset:45312
	ds_read_b64_tr_b16 v[202:203], v221 offset:45824
	ds_read_b64_tr_b16 v[216:217], v221 offset:47360
	ds_read_b64_tr_b16 v[218:219], v221 offset:47872
	s_waitcnt lgkmcnt(4)
	v_mfma_f32_16x16x32_bf16 v[156:159], v[196:199], v[168:171], v[156:159]
	ds_read_b64_tr_b16 v[196:197], v221 offset:49408
	ds_read_b64_tr_b16 v[198:199], v221 offset:49920
	v_pk_mul_f32 v[154:155], v[154:155], v[2:3] op_sel_hi:[1,0]
	v_pk_mul_f32 v[152:153], v[152:153], v[2:3] op_sel_hi:[1,0]
	v_pk_mul_f32 v[150:151], v[150:151], v[2:3] op_sel_hi:[1,0]
	v_pk_mul_f32 v[148:149], v[148:149], v[2:3] op_sel_hi:[1,0]
	v_pk_mul_f32 v[146:147], v[146:147], v[2:3] op_sel_hi:[1,0]
	v_pk_mul_f32 v[144:145], v[144:145], v[2:3] op_sel_hi:[1,0]
	s_waitcnt lgkmcnt(4)
	v_mfma_f32_16x16x32_bf16 v[152:155], v[200:203], v[168:171], v[152:155]
	v_cvt_pk_bf16_f32 v188, v188, v189
	v_cvt_pk_bf16_f32 v189, v190, v191
	v_cvt_pk_bf16_f32 v190, v192, v193
	s_waitcnt lgkmcnt(2)
	v_mfma_f32_16x16x32_bf16 v[148:151], v[216:219], v[168:171], v[148:151]
	v_cvt_pk_bf16_f32 v191, v194, v195
	ds_read_b64_tr_b16 v[192:193], v221 offset:44288
	ds_read_b64_tr_b16 v[194:195], v221 offset:44800
	v_pk_add_f32 v[186:187], v[186:187], v[186:187] op_sel:[0,1] op_sel_hi:[1,0]
	s_waitcnt lgkmcnt(2)
	v_mfma_f32_16x16x32_bf16 v[144:147], v[196:199], v[168:171], v[144:147]
	ds_read_b64_tr_b16 v[168:169], v221 offset:46336
	ds_read_b64_tr_b16 v[170:171], v221 offset:46848
	v_cvt_scalef32_pk_bf16_fp8 v197, v58, 1.0 op_sel:[1,0,0]
	v_cvt_scalef32_pk_bf16_fp8 v196, v58, 1.0
	s_waitcnt lgkmcnt(2)
	v_mfma_f32_16x16x32_bf16 v[156:159], v[192:195], v[188:191], v[156:159]
	v_cvt_scalef32_pk_bf16_fp8 v198, v59, 1.0
	v_cvt_scalef32_pk_bf16_fp8 v199, v59, 1.0 op_sel:[1,0,0]
	s_waitcnt lgkmcnt(0)
	v_mfma_f32_16x16x32_bf16 v[152:155], v[168:171], v[188:191], v[152:155]
	ds_read_b64_tr_b16 v[168:169], v221 offset:48384
	ds_read_b64_tr_b16 v[170:171], v221 offset:48896
	ds_read_b64_tr_b16 v[192:193], v221 offset:50432
	ds_read_b64_tr_b16 v[194:195], v221 offset:50944
	s_waitcnt lgkmcnt(2)
	v_mfma_f32_16x16x32_bf16 v[148:151], v[168:171], v[188:191], v[148:151]
	v_cvt_scalef32_pk_bf16_fp8 v169, v56, 1.0 op_sel:[1,0,0]
	v_cvt_scalef32_pk_bf16_fp8 v168, v56, 1.0
	v_cvt_scalef32_pk_bf16_fp8 v171, v57, 1.0 op_sel:[1,0,0]
	v_cvt_scalef32_pk_bf16_fp8 v170, v57, 1.0
	ds_write_b128 v220, v[168:171] offset:43264
	ds_write_b128 v220, v[196:199] offset:43280
	v_cvt_scalef32_pk_bf16_fp8 v169, v52, 1.0 op_sel:[1,0,0]
	v_cvt_scalef32_pk_bf16_fp8 v168, v52, 1.0
	v_cvt_scalef32_pk_bf16_fp8 v171, v53, 1.0 op_sel:[1,0,0]
	v_cvt_scalef32_pk_bf16_fp8 v170, v53, 1.0
	v_cvt_scalef32_pk_bf16_fp8 v197, v54, 1.0 op_sel:[1,0,0]
	v_cvt_scalef32_pk_bf16_fp8 v196, v54, 1.0
	v_cvt_scalef32_pk_bf16_fp8 v198, v55, 1.0
	v_cvt_scalef32_pk_bf16_fp8 v199, v55, 1.0 op_sel:[1,0,0]
	ds_write_b128 v220, v[168:171] offset:43776
	ds_write_b128 v220, v[196:199] offset:43792
	s_waitcnt vmcnt(1)
	v_cvt_scalef32_pk_bf16_fp8 v169, v64, 1.0 op_sel:[1,0,0]
	v_cvt_scalef32_pk_bf16_fp8 v168, v64, 1.0
	v_cvt_scalef32_pk_bf16_fp8 v171, v65, 1.0 op_sel:[1,0,0]
	v_cvt_scalef32_pk_bf16_fp8 v170, v65, 1.0
	v_cvt_scalef32_pk_bf16_fp8 v197, v66, 1.0 op_sel:[1,0,0]
	v_cvt_scalef32_pk_bf16_fp8 v196, v66, 1.0
	v_cvt_scalef32_pk_bf16_fp8 v198, v67, 1.0
	v_cvt_scalef32_pk_bf16_fp8 v199, v67, 1.0 op_sel:[1,0,0]
	ds_write_b128 v220, v[168:171] offset:44288
	ds_write_b128 v220, v[196:199] offset:44304
	s_waitcnt vmcnt(0)
	v_cvt_scalef32_pk_bf16_fp8 v169, v60, 1.0 op_sel:[1,0,0]
	v_cvt_scalef32_pk_bf16_fp8 v168, v60, 1.0
	v_cvt_scalef32_pk_bf16_fp8 v171, v61, 1.0 op_sel:[1,0,0]
	v_cvt_scalef32_pk_bf16_fp8 v170, v61, 1.0
	v_cvt_scalef32_pk_bf16_fp8 v197, v62, 1.0 op_sel:[1,0,0]
	v_cvt_scalef32_pk_bf16_fp8 v196, v62, 1.0
	v_cvt_scalef32_pk_bf16_fp8 v198, v63, 1.0
	v_cvt_scalef32_pk_bf16_fp8 v199, v63, 1.0 op_sel:[1,0,0]
	ds_write_b128 v220, v[168:171] offset:44800
	ds_write_b128 v220, v[196:199] offset:44816
	v_cvt_pk_bf16_f32 v168, v178, v179
	v_cvt_pk_bf16_f32 v169, v180, v181
	v_cvt_pk_bf16_f32 v170, v182, v183
	v_cvt_pk_bf16_f32 v171, v184, v185
	ds_read_b64_tr_b16 v[178:179], v221 offset:43264
	ds_read_b64_tr_b16 v[180:181], v221 offset:43776
	ds_read_b64_tr_b16 v[182:183], v221 offset:45312
	ds_read_b64_tr_b16 v[184:185], v221 offset:45824
	s_waitcnt lgkmcnt(2)
	v_mfma_f32_16x16x32_bf16 v[156:159], v[178:181], v[168:171], v[156:159]
	s_waitcnt lgkmcnt(0)
	v_mfma_f32_16x16x32_bf16 v[152:155], v[182:185], v[168:171], v[152:155]
	ds_read_b64_tr_b16 v[178:179], v221 offset:47360
	ds_read_b64_tr_b16 v[180:181], v221 offset:47872
	ds_read_b64_tr_b16 v[182:183], v221 offset:49408
	ds_read_b64_tr_b16 v[184:185], v221 offset:49920
	v_mfma_f32_16x16x32_bf16 v[144:147], v[192:195], v[188:191], v[144:147]
	s_waitcnt lgkmcnt(2)
	v_mfma_f32_16x16x32_bf16 v[148:151], v[178:181], v[168:171], v[148:151]
	v_cvt_pk_bf16_f32 v178, v160, v161
	v_cvt_pk_bf16_f32 v179, v162, v163
	v_cvt_pk_bf16_f32 v180, v164, v165
	v_cvt_pk_bf16_f32 v181, v166, v167
	ds_read_b64_tr_b16 v[160:161], v221 offset:44288
	ds_read_b64_tr_b16 v[162:163], v221 offset:44800
	ds_read_b64_tr_b16 v[164:165], v221 offset:46336
	ds_read_b64_tr_b16 v[166:167], v221 offset:46848
	s_waitcnt lgkmcnt(4)
	v_mfma_f32_16x16x32_bf16 v[144:147], v[182:185], v[168:171], v[144:147]
	ds_read_b64_tr_b16 v[168:169], v221 offset:48384
	ds_read_b64_tr_b16 v[170:171], v221 offset:48896
	ds_read_b64_tr_b16 v[182:183], v221 offset:50432
	ds_read_b64_tr_b16 v[184:185], v221 offset:50944
	s_waitcnt lgkmcnt(6)
	v_mfma_f32_16x16x32_bf16 v[156:159], v[160:163], v[178:181], v[156:159]
	v_mov_b32_e32 v160, v186
	s_nop 1
	v_permlane16_swap_b32_e32 v186, v160
	s_waitcnt lgkmcnt(4)
	v_mfma_f32_16x16x32_bf16 v[152:155], v[164:167], v[178:181], v[152:155]
	v_add_f32_e32 v160, v186, v160
	v_mov_b32_e32 v161, v160
	s_nop 1
	v_permlane32_swap_b32_e32 v160, v161
	s_waitcnt lgkmcnt(2)
	v_mfma_f32_16x16x32_bf16 v[148:151], v[168:171], v[178:181], v[148:151]
	s_waitcnt lgkmcnt(0)
	v_mfma_f32_16x16x32_bf16 v[144:147], v[182:185], v[178:181], v[144:147]
	s_cbranch_vccnz .LBB0_1389
	s_branch .Lsb_1389
.LBB0_1389:
	v_add_f32_e32 v160, v160, v161
	v_fmac_f32_e32 v160, v241, v2
	s_cmp_eq_u32 s44, s46
	v_add_u32_e32 v246, 0x200, v246
	s_cbranch_scc0 .LBB0_1371
	v_div_scale_f32 v2, s[0:1], v160, v160, 1.0
	v_rcp_f32_e32 v140, v2
	v_div_scale_f32 v141, vcc, 1.0, v160, 1.0
	s_ashr_i32 s17, s16, 31
	v_fma_f32 v142, -v2, v140, 1.0
	v_fmac_f32_e32 v140, v142, v140
	v_mul_f32_e32 v142, v141, v140
	v_fma_f32 v143, -v2, v142, v141
	v_fmac_f32_e32 v142, v143, v140
	v_fma_f32 v2, -v2, v142, v141
	v_div_fmas_f32 v2, v2, v140, v142
	v_div_fixup_f32 v2, v2, v160, 1.0
	v_mul_f32_e32 v142, v2, v156
	v_mul_f32_e32 v143, v2, v157
	v_mul_f32_e32 v156, v2, v158
	v_mov_b32_e32 v158, v3
	v_cvt_pk_fp8_f32 v158, v142, v143
	v_mul_f32_e32 v142, v2, v152
	v_mul_f32_e32 v143, v2, v153
	v_mov_b32_e32 v152, v3
	v_cvt_pk_fp8_f32 v152, v142, v143
	v_mul_f32_e32 v142, v2, v154
	v_mul_f32_e32 v143, v2, v155
	v_mul_f32_e32 v157, v2, v159
	v_cvt_pk_fp8_f32 v152, v142, v143 op_sel:[0,0,1]
	v_mul_f32_e32 v142, v2, v148
	v_mul_f32_e32 v143, v2, v149
	v_mul_f32_e32 v148, v2, v150
	v_mov_b32_e32 v150, v3
	v_cvt_pk_fp8_f32 v150, v142, v143
	v_mul_f32_e32 v142, v2, v144
	v_mul_f32_e32 v143, v2, v145
	v_mov_b32_e32 v144, v3
	v_cvt_pk_fp8_f32 v144, v142, v143
	v_cvt_pk_fp8_f32 v158, v156, v157 op_sel:[0,0,1]
	v_mul_f32_e32 v149, v2, v151
	s_lshl_b64 s[0:1], s[16:17], 10
	v_cvt_pk_fp8_f32 v150, v148, v149 op_sel:[0,0,1]
	v_mul_f32_e32 v142, v2, v146
	v_mul_f32_e32 v2, v2, v147
	v_lshl_add_u64 v[140:141], v[172:173], 0, s[0:1]
	v_cvt_pk_fp8_f32 v144, v142, v2 op_sel:[0,0,1]
	global_store_dword v[140:141], v158, off
	global_store_dword v[140:141], v152, off offset:16
	global_store_dword v[140:141], v150, off offset:32
	global_store_dword v[140:141], v144, off offset:48
	s_xor_b32 s40, s40, 1
	v_mov_b64_e32 v[146:147], v[138:139]
	v_mov_b64_e32 v[142:143], v[134:135]
	s_cmp_eq_u32 s41, 16
	v_mov_b64_e32 v[144:145], v[136:137]
	v_mov_b64_e32 v[140:141], v[132:133]
	s_mov_b32 s1, s41
	s_cbranch_scc0 .LBB0_1360
	s_branch .Lsp_exit

.Lsb_1385:
	s_andn2_b64 vcc, exec, s[30:31]
	s_mov_b64 s[28:29], 0
	s_cbranch_vccnz .Lsb_1387
	v_lshl_add_u32 v2, v210, 2, s47
	ds_read2_b32 v[12:13], v2 offset0:80 offset1:96
	s_add_u32 s0, s35, s0
	s_addc_u32 s1, s36, s1
	global_load_dwordx4 v[40:43], v186, s[0:1]
	s_mov_b64 s[28:29], -1
	s_waitcnt lgkmcnt(0)
	v_add_u32_e32 v12, v12, v209
	v_add_u32_e32 v13, v13, v209
	global_load_dwordx4 v[36:39], v188, s[0:1]
	global_load_dwordx4 v[48:51], v190, s[0:1]
	global_load_dwordx4 v[44:47], v192, s[0:1]
	global_load_dwordx4 v[56:59], v194, s[0:1]
	global_load_dwordx4 v[52:55], v12, s[0:1]
	global_load_dwordx4 v[64:67], v13, s[0:1]
	global_load_dwordx4 v[8:11], v160, s[0:1]
	global_load_dwordx4 v[4:7], v162, s[0:1]
	global_load_dwordx4 v[16:19], v164, s[0:1]
	s_nop 0
	global_load_dwordx4 v[12:15], v166, s[0:1]
	ds_read_b32 v2, v2 offset:448
	global_load_dwordx4 v[24:27], v178, s[0:1]
	global_load_dwordx4 v[20:23], v180, s[0:1]
	global_load_dwordx4 v[32:35], v182, s[0:1]
	global_load_dwordx4 v[28:31], v184, s[0:1]
	s_waitcnt lgkmcnt(0)
	v_add_u32_e32 v2, v2, v209
	global_load_dwordx4 v[60:63], v2, s[0:1]
.Lsb_1387:
	ds_read_b128 v[160:163], v246
	v_mfma_f32_16x16x32_fp8_fp8 v[164:167], v[80:81], v[174:175], 0
	s_andn2_b64 vcc, exec, s[28:29]
	s_waitcnt lgkmcnt(0)
	v_add_u32_e32 v2, v211, v160
	v_add_u32_e32 v160, v211, v161
	v_add_u32_e32 v161, v211, v162
	v_add_u32_e32 v162, v211, v163
	ds_read_b32 v168, v2 offset:8192
	ds_read_b32 v169, v160 offset:8192
	ds_read_b32 v170, v161 offset:8192
	ds_read_b32 v171, v162 offset:8192
	v_mfma_f32_16x16x32_fp8_fp8 v[160:163], v[82:83], v[176:177], v[164:167]
	s_waitcnt lgkmcnt(2)
	s_nop 6
	v_pk_fma_f32 v[160:161], v[160:161], s[72:73], v[168:169] op_sel_hi:[1,0,1]
	s_waitcnt lgkmcnt(0)
	v_pk_fma_f32 v[162:163], v[162:163], s[72:73], v[170:171] op_sel_hi:[1,0,1]
	s_nop 0
	ds_read_b128 v[164:167], v246 offset:64
	s_waitcnt lgkmcnt(0)
	v_add_u32_e32 v2, v211, v164
	v_add_u32_e32 v169, v211, v165
	v_add_u32_e32 v170, v211, v166
	v_add_u32_e32 v171, v211, v167
	v_mfma_f32_16x16x32_fp8_fp8 v[164:167], v[76:77], v[174:175], 0
	ds_read_b32 v168, v2 offset:8192
	ds_read_b32 v169, v169 offset:8192
	ds_read_b32 v170, v170 offset:8192
	ds_read_b32 v171, v171 offset:8192
	v_mfma_f32_16x16x32_fp8_fp8 v[164:167], v[78:79], v[176:177], v[164:167]
	s_waitcnt lgkmcnt(0)
	s_nop 6
	v_pk_fma_f32 v[166:167], v[166:167], s[72:73], v[170:171] op_sel_hi:[1,0,1]
	v_pk_fma_f32 v[164:165], v[164:165], s[72:73], v[168:169] op_sel_hi:[1,0,1]
	s_nop 0
	ds_read_b128 v[178:181], v246 offset:128
	s_waitcnt lgkmcnt(0)
	v_add_u32_e32 v2, v211, v178
	v_add_u32_e32 v169, v211, v179
	v_add_u32_e32 v170, v211, v180
	v_add_u32_e32 v171, v211, v181
	v_mfma_f32_16x16x32_fp8_fp8 v[178:181], v[72:73], v[174:175], 0
	ds_read_b32 v168, v2 offset:8192
	ds_read_b32 v169, v169 offset:8192
	ds_read_b32 v170, v170 offset:8192
	ds_read_b32 v171, v171 offset:8192
	v_mfma_f32_16x16x32_fp8_fp8 v[178:181], v[74:75], v[176:177], v[178:181]
	s_waitcnt lgkmcnt(0)
	s_nop 6
	v_pk_fma_f32 v[180:181], v[180:181], s[72:73], v[170:171] op_sel_hi:[1,0,1]
	v_pk_fma_f32 v[178:179], v[178:179], s[72:73], v[168:169] op_sel_hi:[1,0,1]
	s_nop 0
	ds_read_b128 v[182:185], v246 offset:192
	s_waitcnt lgkmcnt(0)
	v_add_u32_e32 v2, v211, v182
	v_add_u32_e32 v169, v211, v183
	v_add_u32_e32 v170, v211, v184
	v_add_u32_e32 v171, v211, v185
	v_mfma_f32_16x16x32_fp8_fp8 v[182:185], v[68:69], v[174:175], 0
	ds_read_b32 v168, v2 offset:8192
	ds_read_b32 v169, v169 offset:8192
	ds_read_b32 v170, v170 offset:8192
	ds_read_b32 v171, v171 offset:8192
	v_max3_f32 v2, v160, s33, v161
	v_max3_f32 v2, v2, v162, v163
	v_mfma_f32_16x16x32_fp8_fp8 v[182:185], v[70:71], v[176:177], v[182:185]
	v_max3_f32 v2, v2, v164, v165
	v_max3_f32 v2, v2, v166, v167
	v_max3_f32 v2, v2, v178, v179
	v_max3_f32 v2, v2, v180, v181
	s_waitcnt lgkmcnt(0)
	s_nop 2
	v_pk_fma_f32 v[184:185], v[184:185], s[72:73], v[170:171] op_sel_hi:[1,0,1]
	v_pk_fma_f32 v[182:183], v[182:183], s[72:73], v[168:169] op_sel_hi:[1,0,1]
	s_nop 0
	ds_read_b128 v[186:189], v246 offset:256
	v_max3_f32 v2, v2, v182, v183
	v_max3_f32 v2, v2, v184, v185
	s_waitcnt lgkmcnt(0)
	v_add_u32_e32 v168, v211, v186
	v_add_u32_e32 v169, v211, v187
	v_add_u32_e32 v170, v211, v188
	v_add_u32_e32 v171, v211, v189
	v_mfma_f32_16x16x32_fp8_fp8 v[186:189], v[96:97], v[174:175], 0
	ds_read_b32 v168, v168 offset:8192
	ds_read_b32 v169, v169 offset:8192
	ds_read_b32 v170, v170 offset:8192
	ds_read_b32 v171, v171 offset:8192
	v_mfma_f32_16x16x32_fp8_fp8 v[186:189], v[98:99], v[176:177], v[186:189]
	s_waitcnt lgkmcnt(0)
	s_nop 6
	v_pk_fma_f32 v[236:237], v[188:189], s[72:73], v[170:171] op_sel_hi:[1,0,1]
	v_pk_fma_f32 v[234:235], v[186:187], s[72:73], v[168:169] op_sel_hi:[1,0,1]
	s_nop 0
	ds_read_b128 v[186:189], v246 offset:320
	v_max3_f32 v2, v2, v234, v235
	v_max3_f32 v2, v2, v236, v237
	s_waitcnt lgkmcnt(0)
	v_add_u32_e32 v168, v211, v186
	v_add_u32_e32 v169, v211, v187
	v_add_u32_e32 v170, v211, v188
	v_add_u32_e32 v171, v211, v189
	v_mfma_f32_16x16x32_fp8_fp8 v[186:189], v[92:93], v[174:175], 0
	ds_read_b32 v168, v168 offset:8192
	ds_read_b32 v169, v169 offset:8192
	ds_read_b32 v170, v170 offset:8192
	ds_read_b32 v171, v171 offset:8192
	v_mfma_f32_16x16x32_fp8_fp8 v[186:189], v[94:95], v[176:177], v[186:189]
	s_waitcnt lgkmcnt(0)
	s_nop 6
	v_pk_fma_f32 v[230:231], v[188:189], s[72:73], v[170:171] op_sel_hi:[1,0,1]
	v_pk_fma_f32 v[228:229], v[186:187], s[72:73], v[168:169] op_sel_hi:[1,0,1]
	s_nop 0
	ds_read_b128 v[186:189], v246 offset:384
	v_max3_f32 v2, v2, v228, v229
	v_max3_f32 v2, v2, v230, v231
	s_waitcnt lgkmcnt(0)
	v_add_u32_e32 v168, v211, v186
	v_add_u32_e32 v169, v211, v187
	v_add_u32_e32 v170, v211, v188
	v_add_u32_e32 v171, v211, v189
	v_mfma_f32_16x16x32_fp8_fp8 v[186:189], v[88:89], v[174:175], 0
	ds_read_b32 v168, v168 offset:8192
	ds_read_b32 v169, v169 offset:8192
	ds_read_b32 v170, v170 offset:8192
	ds_read_b32 v171, v171 offset:8192
	v_mfma_f32_16x16x32_fp8_fp8 v[186:189], v[90:91], v[176:177], v[186:189]
	s_waitcnt lgkmcnt(0)
	s_nop 6
	v_pk_fma_f32 v[170:171], v[188:189], s[72:73], v[170:171] op_sel_hi:[1,0,1]
	v_pk_fma_f32 v[168:169], v[186:187], s[72:73], v[168:169] op_sel_hi:[1,0,1]
	s_nop 0
	ds_read_b128 v[186:189], v246 offset:448
	v_max3_f32 v2, v2, v168, v169
	v_max3_f32 v2, v2, v170, v171
	s_waitcnt lgkmcnt(0)
	v_add_u32_e32 v190, v211, v186
	v_add_u32_e32 v191, v211, v187
	v_add_u32_e32 v192, v211, v188
	v_add_u32_e32 v193, v211, v189
	v_mfma_f32_16x16x32_fp8_fp8 v[186:189], v[84:85], v[174:175], 0
	ds_read_b32 v190, v190 offset:8192
	ds_read_b32 v191, v191 offset:8192
	ds_read_b32 v192, v192 offset:8192
	ds_read_b32 v193, v193 offset:8192
	v_mfma_f32_16x16x32_fp8_fp8 v[186:189], v[86:87], v[176:177], v[186:189]
	s_waitcnt lgkmcnt(0)
	s_nop 6
	v_pk_fma_f32 v[218:219], v[188:189], s[72:73], v[192:193] op_sel_hi:[1,0,1]
	v_pk_fma_f32 v[216:217], v[186:187], s[72:73], v[190:191] op_sel_hi:[1,0,1]
	s_nop 0
	s_nop 0
	v_max3_f32 v2, v2, v216, v217
	v_max3_f32 v2, v2, v218, v219
	v_mov_b32_e32 v186, v2
	s_nop 1
	v_permlane16_swap_b32_e32 v2, v186
	v_max_f32_e32 v186, v186, v186
	v_max_f32_e32 v2, v2, v2
	v_max_f32_e32 v2, v2, v186
	v_mov_b32_e32 v186, v2
	s_nop 1
	v_permlane32_swap_b32_e32 v2, v186
	v_max3_f32 v214, v196, v2, v186
	v_sub_f32_e32 v163, v163, v214
	v_sub_f32_e32 v162, v162, v214
	v_sub_f32_e32 v161, v161, v214
	v_sub_f32_e32 v160, v160, v214
	v_sub_f32_e32 v2, v196, v214
	v_exp_f32_e32 v196, v160
	v_exp_f32_e32 v197, v161
	v_exp_f32_e32 v198, v162
	v_exp_f32_e32 v199, v163
	v_sub_f32_e32 v163, v167, v214
	v_sub_f32_e32 v162, v166, v214
	v_sub_f32_e32 v161, v165, v214
	v_sub_f32_e32 v160, v164, v214
	v_sub_f32_e32 v167, v219, v214
	v_exp_f32_e32 v200, v160
	v_exp_f32_e32 v201, v161
	v_exp_f32_e32 v202, v162
	v_exp_f32_e32 v203, v163
	v_sub_f32_e32 v163, v181, v214
	v_sub_f32_e32 v162, v180, v214
	v_sub_f32_e32 v161, v179, v214
	v_sub_f32_e32 v160, v178, v214
	v_sub_f32_e32 v166, v218, v214
	v_exp_f32_e32 v188, v160
	v_exp_f32_e32 v189, v161
	v_exp_f32_e32 v190, v162
	v_exp_f32_e32 v191, v163
	v_sub_f32_e32 v163, v185, v214
	v_sub_f32_e32 v162, v184, v214
	v_sub_f32_e32 v161, v183, v214
	v_sub_f32_e32 v160, v182, v214
	v_sub_f32_e32 v165, v217, v214
	v_exp_f32_e32 v192, v160
	v_exp_f32_e32 v193, v161
	v_exp_f32_e32 v194, v162
	v_exp_f32_e32 v195, v163
	v_sub_f32_e32 v163, v237, v214
	v_sub_f32_e32 v162, v236, v214
	v_sub_f32_e32 v161, v235, v214
	v_sub_f32_e32 v160, v234, v214
	v_sub_f32_e32 v164, v216, v214
	v_exp_f32_e32 v178, v160
	v_exp_f32_e32 v179, v161
	v_exp_f32_e32 v180, v162
	v_exp_f32_e32 v181, v163
	v_sub_f32_e32 v163, v231, v214
	v_sub_f32_e32 v162, v230, v214
	v_sub_f32_e32 v161, v229, v214
	v_sub_f32_e32 v160, v228, v214
	v_pk_add_f32 v[218:219], v[190:191], v[194:195]
	v_exp_f32_e32 v182, v160
	v_exp_f32_e32 v183, v161
	v_exp_f32_e32 v184, v162
	v_exp_f32_e32 v185, v163
	v_sub_f32_e32 v163, v171, v214
	v_sub_f32_e32 v162, v170, v214
	v_sub_f32_e32 v161, v169, v214
	v_sub_f32_e32 v160, v168, v214
	v_pk_add_f32 v[170:171], v[198:199], v[202:203]
	v_exp_f32_e32 v160, v160
	v_exp_f32_e32 v161, v161
	v_exp_f32_e32 v162, v162
	v_exp_f32_e32 v163, v163
	v_exp_f32_e32 v164, v164
	v_exp_f32_e32 v165, v165
	v_exp_f32_e32 v166, v166
	v_exp_f32_e32 v167, v167
	v_pk_add_f32 v[168:169], v[196:197], v[200:201]
	v_pk_add_f32 v[216:217], v[188:189], v[192:193]
	v_pk_add_f32 v[230:231], v[180:181], v[184:185]
	v_pk_add_f32 v[228:229], v[178:179], v[182:183]
	v_pk_add_f32 v[236:237], v[162:163], v[166:167]
	v_pk_add_f32 v[234:235], v[160:161], v[164:165]
	v_exp_f32_e32 v2, v2
	s_nop 0
	v_pk_add_f32 v[170:171], v[170:171], v[218:219]
	v_pk_add_f32 v[168:169], v[168:169], v[216:217]
	v_pk_add_f32 v[218:219], v[230:231], v[236:237]
	v_pk_add_f32 v[216:217], v[228:229], v[234:235]
	v_pk_mul_f32 v[158:159], v[158:159], v[2:3] op_sel_hi:[1,0]
	v_pk_mul_f32 v[156:157], v[156:157], v[2:3] op_sel_hi:[1,0]
	v_pk_add_f32 v[170:171], v[170:171], v[218:219]
	v_pk_add_f32 v[168:169], v[168:169], v[216:217]
	v_cvt_scalef32_pk_bf16_fp8 v217, v102, 1.0 op_sel:[1,0,0]
	v_cvt_scalef32_pk_bf16_fp8 v216, v102, 1.0
	v_pk_add_f32 v[186:187], v[168:169], v[170:171]
	v_cvt_scalef32_pk_bf16_fp8 v169, v100, 1.0 op_sel:[1,0,0]
	v_cvt_scalef32_pk_bf16_fp8 v168, v100, 1.0
	v_cvt_scalef32_pk_bf16_fp8 v171, v101, 1.0 op_sel:[1,0,0]
	v_cvt_scalef32_pk_bf16_fp8 v170, v101, 1.0
	v_cvt_scalef32_pk_bf16_fp8 v218, v103, 1.0
	v_cvt_scalef32_pk_bf16_fp8 v219, v103, 1.0 op_sel:[1,0,0]
	ds_write_b128 v220, v[168:171] offset:43264
	ds_write_b128 v220, v[216:219] offset:43280
	v_cvt_scalef32_pk_bf16_fp8 v169, v124, 1.0 op_sel:[1,0,0]
	v_cvt_scalef32_pk_bf16_fp8 v168, v124, 1.0
	v_cvt_scalef32_pk_bf16_fp8 v171, v125, 1.0 op_sel:[1,0,0]
	v_cvt_scalef32_pk_bf16_fp8 v170, v125, 1.0
	v_cvt_scalef32_pk_bf16_fp8 v217, v126, 1.0 op_sel:[1,0,0]
	v_cvt_scalef32_pk_bf16_fp8 v216, v126, 1.0
	v_cvt_scalef32_pk_bf16_fp8 v218, v127, 1.0
	v_cvt_scalef32_pk_bf16_fp8 v219, v127, 1.0 op_sel:[1,0,0]
	ds_write_b128 v220, v[168:171] offset:43776
	ds_write_b128 v220, v[216:219] offset:43792
	v_cvt_scalef32_pk_bf16_fp8 v169, v120, 1.0 op_sel:[1,0,0]
	v_cvt_scalef32_pk_bf16_fp8 v168, v120, 1.0
	v_cvt_scalef32_pk_bf16_fp8 v171, v121, 1.0 op_sel:[1,0,0]
	v_cvt_scalef32_pk_bf16_fp8 v170, v121, 1.0
	v_cvt_scalef32_pk_bf16_fp8 v217, v122, 1.0 op_sel:[1,0,0]
	v_cvt_scalef32_pk_bf16_fp8 v216, v122, 1.0
	v_cvt_scalef32_pk_bf16_fp8 v218, v123, 1.0
	v_cvt_scalef32_pk_bf16_fp8 v219, v123, 1.0 op_sel:[1,0,0]
	ds_write_b128 v220, v[168:171] offset:44288
	ds_write_b128 v220, v[216:219] offset:44304
	v_cvt_scalef32_pk_bf16_fp8 v169, v116, 1.0 op_sel:[1,0,0]
	v_cvt_scalef32_pk_bf16_fp8 v168, v116, 1.0
	v_cvt_scalef32_pk_bf16_fp8 v171, v117, 1.0 op_sel:[1,0,0]
	v_cvt_scalef32_pk_bf16_fp8 v170, v117, 1.0
	v_cvt_scalef32_pk_bf16_fp8 v217, v118, 1.0 op_sel:[1,0,0]
	v_cvt_scalef32_pk_bf16_fp8 v216, v118, 1.0
	v_cvt_scalef32_pk_bf16_fp8 v218, v119, 1.0
	v_cvt_scalef32_pk_bf16_fp8 v219, v119, 1.0 op_sel:[1,0,0]
	ds_write_b128 v220, v[168:171] offset:44800
	ds_write_b128 v220, v[216:219] offset:44816
	v_cvt_pk_bf16_f32 v168, v196, v197
	v_cvt_pk_bf16_f32 v169, v198, v199
	v_cvt_pk_bf16_f32 v170, v200, v201
	v_cvt_pk_bf16_f32 v171, v202, v203
	ds_read_b64_tr_b16 v[196:197], v221 offset:43264
	ds_read_b64_tr_b16 v[198:199], v221 offset:43776
	ds_read_b64_tr_b16 v[200:201], v221 offset:45312
	ds_read_b64_tr_b16 v[202:203], v221 offset:45824
	ds_read_b64_tr_b16 v[216:217], v221 offset:47360
	ds_read_b64_tr_b16 v[218:219], v221 offset:47872
	s_waitcnt lgkmcnt(4)
	v_mfma_f32_16x16x32_bf16 v[156:159], v[196:199], v[168:171], v[156:159]
	ds_read_b64_tr_b16 v[196:197], v221 offset:49408
	ds_read_b64_tr_b16 v[198:199], v221 offset:49920
	v_pk_mul_f32 v[154:155], v[154:155], v[2:3] op_sel_hi:[1,0]
	v_pk_mul_f32 v[152:153], v[152:153], v[2:3] op_sel_hi:[1,0]
	v_pk_mul_f32 v[150:151], v[150:151], v[2:3] op_sel_hi:[1,0]
	v_pk_mul_f32 v[148:149], v[148:149], v[2:3] op_sel_hi:[1,0]
	v_pk_mul_f32 v[146:147], v[146:147], v[2:3] op_sel_hi:[1,0]
	v_pk_mul_f32 v[144:145], v[144:145], v[2:3] op_sel_hi:[1,0]
	s_waitcnt lgkmcnt(4)
	v_mfma_f32_16x16x32_bf16 v[152:155], v[200:203], v[168:171], v[152:155]
	v_cvt_pk_bf16_f32 v188, v188, v189
	v_cvt_pk_bf16_f32 v189, v190, v191
	v_cvt_pk_bf16_f32 v190, v192, v193
	s_waitcnt lgkmcnt(2)
	v_mfma_f32_16x16x32_bf16 v[148:151], v[216:219], v[168:171], v[148:151]
	v_cvt_pk_bf16_f32 v191, v194, v195
	ds_read_b64_tr_b16 v[192:193], v221 offset:44288
	ds_read_b64_tr_b16 v[194:195], v221 offset:44800
	v_pk_add_f32 v[186:187], v[186:187], v[186:187] op_sel:[0,1] op_sel_hi:[1,0]
	s_waitcnt lgkmcnt(2)
	v_mfma_f32_16x16x32_bf16 v[144:147], v[196:199], v[168:171], v[144:147]
	ds_read_b64_tr_b16 v[168:169], v221 offset:46336
	ds_read_b64_tr_b16 v[170:171], v221 offset:46848
	v_cvt_scalef32_pk_bf16_fp8 v197, v114, 1.0 op_sel:[1,0,0]
	v_cvt_scalef32_pk_bf16_fp8 v196, v114, 1.0
	s_waitcnt lgkmcnt(2)
	v_mfma_f32_16x16x32_bf16 v[156:159], v[192:195], v[188:191], v[156:159]
	v_cvt_scalef32_pk_bf16_fp8 v198, v115, 1.0
	v_cvt_scalef32_pk_bf16_fp8 v199, v115, 1.0 op_sel:[1,0,0]
	s_waitcnt lgkmcnt(0)
	v_mfma_f32_16x16x32_bf16 v[152:155], v[168:171], v[188:191], v[152:155]
	ds_read_b64_tr_b16 v[168:169], v221 offset:48384
	ds_read_b64_tr_b16 v[170:171], v221 offset:48896
	ds_read_b64_tr_b16 v[192:193], v221 offset:50432
	ds_read_b64_tr_b16 v[194:195], v221 offset:50944
	s_waitcnt lgkmcnt(2)
	v_mfma_f32_16x16x32_bf16 v[148:151], v[168:171], v[188:191], v[148:151]
	v_cvt_scalef32_pk_bf16_fp8 v169, v112, 1.0 op_sel:[1,0,0]
	v_cvt_scalef32_pk_bf16_fp8 v168, v112, 1.0
	v_cvt_scalef32_pk_bf16_fp8 v171, v113, 1.0 op_sel:[1,0,0]
	v_cvt_scalef32_pk_bf16_fp8 v170, v113, 1.0
	ds_write_b128 v220, v[168:171] offset:43264
	ds_write_b128 v220, v[196:199] offset:43280
	v_cvt_scalef32_pk_bf16_fp8 v169, v108, 1.0 op_sel:[1,0,0]
	v_cvt_scalef32_pk_bf16_fp8 v168, v108, 1.0
	v_cvt_scalef32_pk_bf16_fp8 v171, v109, 1.0 op_sel:[1,0,0]
	v_cvt_scalef32_pk_bf16_fp8 v170, v109, 1.0
	v_cvt_scalef32_pk_bf16_fp8 v197, v110, 1.0 op_sel:[1,0,0]
	v_cvt_scalef32_pk_bf16_fp8 v196, v110, 1.0
	v_cvt_scalef32_pk_bf16_fp8 v198, v111, 1.0
	v_cvt_scalef32_pk_bf16_fp8 v199, v111, 1.0 op_sel:[1,0,0]
	ds_write_b128 v220, v[168:171] offset:43776
	ds_write_b128 v220, v[196:199] offset:43792
	s_waitcnt vmcnt(1)
	v_cvt_scalef32_pk_bf16_fp8 v169, v104, 1.0 op_sel:[1,0,0]
	v_cvt_scalef32_pk_bf16_fp8 v168, v104, 1.0
	v_cvt_scalef32_pk_bf16_fp8 v171, v105, 1.0 op_sel:[1,0,0]
	v_cvt_scalef32_pk_bf16_fp8 v170, v105, 1.0
	v_cvt_scalef32_pk_bf16_fp8 v197, v106, 1.0 op_sel:[1,0,0]
	v_cvt_scalef32_pk_bf16_fp8 v196, v106, 1.0
	v_cvt_scalef32_pk_bf16_fp8 v198, v107, 1.0
	v_cvt_scalef32_pk_bf16_fp8 v199, v107, 1.0 op_sel:[1,0,0]
	ds_write_b128 v220, v[168:171] offset:44288
	ds_write_b128 v220, v[196:199] offset:44304
	s_waitcnt vmcnt(0)
	v_cvt_scalef32_pk_bf16_fp8 v169, v128, 1.0 op_sel:[1,0,0]
	v_cvt_scalef32_pk_bf16_fp8 v168, v128, 1.0
	v_cvt_scalef32_pk_bf16_fp8 v171, v129, 1.0 op_sel:[1,0,0]
	v_cvt_scalef32_pk_bf16_fp8 v170, v129, 1.0
	v_cvt_scalef32_pk_bf16_fp8 v197, v130, 1.0 op_sel:[1,0,0]
	v_cvt_scalef32_pk_bf16_fp8 v196, v130, 1.0
	v_cvt_scalef32_pk_bf16_fp8 v198, v131, 1.0
	v_cvt_scalef32_pk_bf16_fp8 v199, v131, 1.0 op_sel:[1,0,0]
	ds_write_b128 v220, v[168:171] offset:44800
	ds_write_b128 v220, v[196:199] offset:44816
	v_cvt_pk_bf16_f32 v168, v178, v179
	v_cvt_pk_bf16_f32 v169, v180, v181
	v_cvt_pk_bf16_f32 v170, v182, v183
	v_cvt_pk_bf16_f32 v171, v184, v185
	ds_read_b64_tr_b16 v[178:179], v221 offset:43264
	ds_read_b64_tr_b16 v[180:181], v221 offset:43776
	ds_read_b64_tr_b16 v[182:183], v221 offset:45312
	ds_read_b64_tr_b16 v[184:185], v221 offset:45824
	s_waitcnt lgkmcnt(2)
	v_mfma_f32_16x16x32_bf16 v[156:159], v[178:181], v[168:171], v[156:159]
	s_waitcnt lgkmcnt(0)
	v_mfma_f32_16x16x32_bf16 v[152:155], v[182:185], v[168:171], v[152:155]
	ds_read_b64_tr_b16 v[178:179], v221 offset:47360
	ds_read_b64_tr_b16 v[180:181], v221 offset:47872
	ds_read_b64_tr_b16 v[182:183], v221 offset:49408
	ds_read_b64_tr_b16 v[184:185], v221 offset:49920
	v_mfma_f32_16x16x32_bf16 v[144:147], v[192:195], v[188:191], v[144:147]
	s_waitcnt lgkmcnt(2)
	v_mfma_f32_16x16x32_bf16 v[148:151], v[178:181], v[168:171], v[148:151]
	v_cvt_pk_bf16_f32 v178, v160, v161
	v_cvt_pk_bf16_f32 v179, v162, v163
	v_cvt_pk_bf16_f32 v180, v164, v165
	v_cvt_pk_bf16_f32 v181, v166, v167
	ds_read_b64_tr_b16 v[160:161], v221 offset:44288
	ds_read_b64_tr_b16 v[162:163], v221 offset:44800
	ds_read_b64_tr_b16 v[164:165], v221 offset:46336
	ds_read_b64_tr_b16 v[166:167], v221 offset:46848
	s_waitcnt lgkmcnt(4)
	v_mfma_f32_16x16x32_bf16 v[144:147], v[182:185], v[168:171], v[144:147]
	ds_read_b64_tr_b16 v[168:169], v221 offset:48384
	ds_read_b64_tr_b16 v[170:171], v221 offset:48896
	ds_read_b64_tr_b16 v[182:183], v221 offset:50432
	ds_read_b64_tr_b16 v[184:185], v221 offset:50944
	s_waitcnt lgkmcnt(6)
	v_mfma_f32_16x16x32_bf16 v[156:159], v[160:163], v[178:181], v[156:159]
	v_mov_b32_e32 v160, v186
	s_nop 1
	v_permlane16_swap_b32_e32 v186, v160
	s_waitcnt lgkmcnt(4)
	v_mfma_f32_16x16x32_bf16 v[152:155], v[164:167], v[178:181], v[152:155]
	v_add_f32_e32 v160, v186, v160
	v_mov_b32_e32 v161, v160
	s_nop 1
	v_permlane32_swap_b32_e32 v160, v161
	s_waitcnt lgkmcnt(2)
	v_mfma_f32_16x16x32_bf16 v[148:151], v[168:171], v[178:181], v[148:151]
	s_waitcnt lgkmcnt(0)
	v_mfma_f32_16x16x32_bf16 v[144:147], v[182:185], v[178:181], v[144:147]
	s_cbranch_vccnz .Lsb_1389
	s_branch .LBB0_1389
.Lsb_1389:
	v_add_f32_e32 v160, v160, v161
	v_fmac_f32_e32 v160, v241, v2
	s_cmp_eq_u32 s44, s46
	v_add_u32_e32 v246, 0x200, v246
	s_cbranch_scc0 .Lsb_1371
	v_div_scale_f32 v2, s[0:1], v160, v160, 1.0
	v_rcp_f32_e32 v140, v2
	v_div_scale_f32 v141, vcc, 1.0, v160, 1.0
	s_ashr_i32 s17, s16, 31
	v_fma_f32 v142, -v2, v140, 1.0
	v_fmac_f32_e32 v140, v142, v140
	v_mul_f32_e32 v142, v141, v140
	v_fma_f32 v143, -v2, v142, v141
	v_fmac_f32_e32 v142, v143, v140
	v_fma_f32 v2, -v2, v142, v141
	v_div_fmas_f32 v2, v2, v140, v142
	v_div_fixup_f32 v2, v2, v160, 1.0
	v_mul_f32_e32 v142, v2, v156
	v_mul_f32_e32 v143, v2, v157
	v_mul_f32_e32 v156, v2, v158
	v_mov_b32_e32 v158, v3
	v_cvt_pk_fp8_f32 v158, v142, v143
	v_mul_f32_e32 v142, v2, v152
	v_mul_f32_e32 v143, v2, v153
	v_mov_b32_e32 v152, v3
	v_cvt_pk_fp8_f32 v152, v142, v143
	v_mul_f32_e32 v142, v2, v154
	v_mul_f32_e32 v143, v2, v155
	v_mul_f32_e32 v157, v2, v159
	v_cvt_pk_fp8_f32 v152, v142, v143 op_sel:[0,0,1]
	v_mul_f32_e32 v142, v2, v148
	v_mul_f32_e32 v143, v2, v149
	v_mul_f32_e32 v148, v2, v150
	v_mov_b32_e32 v150, v3
	v_cvt_pk_fp8_f32 v150, v142, v143
	v_mul_f32_e32 v142, v2, v144
	v_mul_f32_e32 v143, v2, v145
	v_mov_b32_e32 v144, v3
	v_cvt_pk_fp8_f32 v144, v142, v143
	v_cvt_pk_fp8_f32 v158, v156, v157 op_sel:[0,0,1]
	v_mul_f32_e32 v149, v2, v151
	s_lshl_b64 s[0:1], s[16:17], 10
	v_cvt_pk_fp8_f32 v150, v148, v149 op_sel:[0,0,1]
	v_mul_f32_e32 v142, v2, v146
	v_mul_f32_e32 v2, v2, v147
	v_lshl_add_u64 v[140:141], v[172:173], 0, s[0:1]
	v_cvt_pk_fp8_f32 v144, v142, v2 op_sel:[0,0,1]
	global_store_dword v[140:141], v158, off
	global_store_dword v[140:141], v152, off offset:16
	global_store_dword v[140:141], v150, off offset:32
	global_store_dword v[140:141], v144, off offset:48
	s_xor_b32 s40, s40, 1
	v_mov_b64_e32 v[146:147], v[138:139]
	v_mov_b64_e32 v[142:143], v[134:135]
	s_cmp_eq_u32 s41, 16
	v_mov_b64_e32 v[144:145], v[136:137]
	v_mov_b64_e32 v[140:141], v[132:133]
	s_mov_b32 s1, s41
	s_cbranch_scc0 .Lsb_1360
.Lsp_exit:
	s_getreg_b32 s0, hwreg(HW_REG_XCC_ID, 0, 4)
	s_waitcnt vmcnt(0)
	s_barrier
	s_mov_b64 s[8:9], exec
	v_readlane_b32 s10, v254, 5
	v_readlane_b32 s11, v254, 6
	s_and_b64 s[10:11], s[8:9], s[10:11]
	s_mov_b64 exec, s[10:11]
	s_cbranch_execz .LBB0_1443
	v_readlane_b32 s1, v254, 13
	s_waitcnt vmcnt(0) expcnt(0) lgkmcnt(0)
	s_and_b32 s3, s0, 15
	v_mov_b32_e32 v1, s1
	ds_read_b32 v4, v1
	v_readlane_b32 s1, v254, 14
	s_waitcnt lgkmcnt(0)
	v_cmp_ne_u32_e32 vcc, 0, v4
	v_mov_b32_e32 v1, s1
	ds_read_b32 v2, v1
	s_cbranch_vccnz .LBB0_1407
	v_readlane_b32 s10, v254, 3
	v_readlane_b32 s11, v254, 4
	s_load_dwordx2 s[0:1], s[10:11], 0x4
	s_add_u32 s10, s64, 0x39801200
	s_addc_u32 s11, s65, 0
	s_add_u32 s12, s64, 0x39801400
	s_addc_u32 s13, s65, 0
	v_readlane_b32 s14, v254, 0
	s_waitcnt lgkmcnt(0)
	s_mul_i32 s50, s0, s14
	s_add_u32 s14, s64, 0x39801500
	s_addc_u32 s15, s65, 0
	s_add_u32 s16, s64, 0x39801600
	s_addc_u32 s17, s65, 0
	s_add_u32 s18, s64, 0x39801700
	s_addc_u32 s19, s65, 0
	s_add_u32 s20, s64, 0x39801800
	s_addc_u32 s21, s65, 0
	s_add_u32 s22, s64, 0x39801900
	s_addc_u32 s23, s65, 0
	s_add_u32 s24, s64, 0x39801a00
	s_addc_u32 s25, s65, 0
	s_add_u32 s26, s64, 0x39801b00
	s_addc_u32 s27, s65, 0
	s_add_u32 s28, s64, 0x39801c00
	s_addc_u32 s29, s65, 0
	s_add_u32 s30, s64, 0x39801d00
	s_addc_u32 s31, s65, 0
	s_add_u32 s34, s64, 0x39801e00
	s_addc_u32 s35, s65, 0
	s_add_u32 s36, s64, 0x39801f00
	s_addc_u32 s37, s65, 0
	s_add_u32 s38, s64, 0x39802000
	s_addc_u32 s39, s65, 0
	s_add_u32 s40, s64, 0x39802100
	s_addc_u32 s41, s65, 0
	s_add_u32 s42, s64, 0x39802200
	s_addc_u32 s43, s65, 0
	s_add_u32 s44, s64, 0x39802300
	s_mul_i32 s50, s50, s1
	s_addc_u32 s45, s65, 0
	s_mov_b32 s51, 1
	s_branch .LBB0_1395
